# v39 + GEMM2: whole fp8 pack of the ai=0 accumulators (64 clamps + 32 converts) done in place between the fourth-phase MFMAs, epilogue ds_writes read the accumulator registers
# speedup vs baseline: 1.0151x; 1.0023x over previous
; #define PG8_STAGE(bufoff, gbase, voff) do { _Pragma("unroll") for (int _i = 0; _i < 2; ++_i) \
;         __builtin_amdgcn_global_load_lds((const unsigned*)((const char*)(gbase) + (voff)[_i]), (LAS unsigned*)(lds + (bufoff) + ldsw + _i * 8192), 16, 0, 0); } while (0)
; #define PG8_LDA(dst, b, h) do { _Pragma("unroll") for (int m = 0; m < 4; ++m) _Pragma("unroll") for (int k = 0; k < 2; ++k) dst[m][k] = *(const LAS bf16x8*)(lds + PG8_SA(b, h) + aoff + m * 2048 + k * 1024); } while (0)
;     ...
;             if constexpr (SP2) {
;             PG8_LDB(B0, 0, 0); PG8_LDB(B1, 0, 1); PG8_SCHED; PG8_LDA(At, 0, 0); PG8_STAGE(PG8_SA(1, 1), a1 + ah, VA1);
;             PG8_WAIT_V(8); PG8_WAIT_L(0); PG8_BAR; PG8_MMA(0, 0, At, B0); PG8_MMA(0, 1, At, B1); PG8_BAR; PG8_SCHED;
;             PG8_LDA(At, 0, 1); PG8_STAGE(PG8_SB(0, 0), b2, voffB); PG8_STAGE(PG8_SB(0, 1), b2 + bstep, voffB); PG8_STAGE(PG8_SA(0, 0), a2, v2[0]);
;             PG8_WAIT_V(8); PG8_WAIT_L(0); PG8_BAR; if (full) { PG8_MMA(1, 0, At, B0); PG8_MMA(1, 1, At, B1); } PG8_BAR; PG8_SCHED;
;             PG8_LDB(B0, 1, 0); PG8_LDB(B1, 1, 1); PG8_SCHED; PG8_LDA(At, 1, 0); PG8_STAGE(PG8_SA(0, 1), a2 + ah, v2[1]);
;             PG8_WAIT_V(8); PG8_WAIT_L(0); PG8_BAR; PG8_MMA(0, 0, At, B0); PG8_MMA(0, 1, At, B1); PG8_BAR; PG8_SCHED;
;             PG8_LDA(At, 1, 1); PG8_STAGE(PG8_SB(1, 0), b3, voffB); PG8_STAGE(PG8_SB(1, 1), b3 + bstep, voffB); PG8_STAGE(PG8_SA(1, 0), a3, v2[0]);
;             PG8_WAIT_V(8); PG8_WAIT_L(0); PG8_BAR; if (full) { PG8_MMA(1, 0, At, B0); PG8_MMA(1, 1, At, B1); } PG8_BAR; PG8_SCHED;
;     __device__ __forceinline__ u32x4 pack(const f32x4 (&acc)[2][2][4][2], int ai, int m) const {
;         u32x4 w;
; #pragma unroll
;         for (int bj = 0; bj < 2; ++bj) {
;             f32x4 v0 = acc[ai][bj][m][0], v1 = acc[ai][bj][m][1];
; #pragma unroll
;             for (int j = 0; j < 4; ++j) { v0[j] = fminf(fmaxf(v0[j], -448.f), 448.f); v1[j] = fminf(fmaxf(v1[j], -448.f), 448.f); }
;             int w0 = __builtin_amdgcn_cvt_pk_fp8_f32(v0[0], v0[1], 0, false); w0 = __builtin_amdgcn_cvt_pk_fp8_f32(v0[2], v0[3], w0, true);
;             int w1 = __builtin_amdgcn_cvt_pk_fp8_f32(v1[0], v1[1], 0, false); w1 = __builtin_amdgcn_cvt_pk_fp8_f32(v1[2], v1[3], w1, true);
;             if (bj == 0) { w.x = (unsigned)w0; w.y = (unsigned)w1; } else { w.z = (unsigned)w0; w.w = (unsigned)w1; } }
.LBB0_841:
	s_add_u32 s4, s4, 0x8000
	s_addc_u32 s5, s5, 0
	s_barrier
	s_add_i32 s35, 0, 0x18000
	s_add_i32 s36, 0, 0x1c000
	v_add_u32_e32 v2, s35, v247
	v_add_u32_e32 v6, s36, v247
	ds_read_b128 v[26:29], v2
	ds_read_b128 v[30:33], v2 offset:1024
	ds_read_b128 v[18:21], v2 offset:2048
	ds_read_b128 v[22:25], v2 offset:3072
	ds_read_b128 v[10:13], v6
	ds_read_b128 v[14:17], v6 offset:1024
	ds_read_b128 v[2:5], v6 offset:2048
	ds_read_b128 v[6:9], v6 offset:3072
	s_mov_b32 m0, s15
	v_lshl_add_u64 v[250:251], s[4:5], 0, v[200:201]
	s_waitcnt lgkmcnt(0)
	ds_read_b128 v[34:37], v223 offset:32768
	ds_read_b128 v[38:41], v223 offset:33792
	ds_read_b128 v[42:45], v223 offset:34816
	ds_read_b128 v[46:49], v223 offset:35840
	ds_read_b128 v[50:53], v223 offset:36864
	ds_read_b128 v[54:57], v223 offset:37888
	ds_read_b128 v[58:61], v223 offset:38912
	ds_read_b128 v[62:65], v223 offset:39936
	global_load_lds_dwordx4 v[250:251], off
	v_lshl_add_u64 v[250:251], s[4:5], 0, v[202:203]
	s_mov_b32 m0, s16
	s_nop 0
	global_load_lds_dwordx4 v[250:251], off
	s_waitcnt vmcnt(8)
	s_waitcnt lgkmcnt(0)
	s_barrier
	s_setprio 1
	s_waitcnt lgkmcnt(0)
	v_mfma_scale_f32_16x16x128_f8f6f4 v[172:175], v[26:33], v[34:41], v[172:175], v1, v246 op_sel_hi:[0,0,0]
	v_mfma_scale_f32_16x16x128_f8f6f4 v[176:179], v[18:25], v[34:41], v[176:179], v1, v246 op_sel_hi:[0,0,0]
	v_mfma_scale_f32_16x16x128_f8f6f4 v[168:171], v[26:33], v[42:49], v[168:171], v1, v246 op_sel_hi:[0,0,0]
	v_mfma_scale_f32_16x16x128_f8f6f4 v[164:167], v[18:25], v[42:49], v[164:167], v1, v246 op_sel_hi:[0,0,0]
	v_mfma_scale_f32_16x16x128_f8f6f4 v[144:147], v[26:33], v[50:57], v[144:147], v1, v246 op_sel_hi:[0,0,0]
	v_mfma_scale_f32_16x16x128_f8f6f4 v[136:139], v[18:25], v[50:57], v[136:139], v1, v246 op_sel_hi:[0,0,0]
	v_mfma_scale_f32_16x16x128_f8f6f4 v[116:119], v[26:33], v[58:65], v[116:119], v1, v246 op_sel_hi:[0,0,0]
	v_mfma_scale_f32_16x16x128_f8f6f4 v[112:115], v[18:25], v[58:65], v[112:115], v1, v246 op_sel_hi:[0,0,0]
	s_setprio 0
	s_setprio 1
	v_mfma_scale_f32_16x16x128_f8f6f4 v[188:191], v[10:17], v[34:41], v[188:191], v1, v246 op_sel_hi:[0,0,0]
	v_mfma_scale_f32_16x16x128_f8f6f4 v[192:195], v[2:9], v[34:41], v[192:195], v1, v246 op_sel_hi:[0,0,0]
	v_mfma_scale_f32_16x16x128_f8f6f4 v[184:187], v[10:17], v[42:49], v[184:187], v1, v246 op_sel_hi:[0,0,0]
	v_mfma_scale_f32_16x16x128_f8f6f4 v[180:183], v[2:9], v[42:49], v[180:183], v1, v246 op_sel_hi:[0,0,0]
	v_mfma_scale_f32_16x16x128_f8f6f4 v[152:155], v[10:17], v[50:57], v[152:155], v1, v246 op_sel_hi:[0,0,0]
	v_mfma_scale_f32_16x16x128_f8f6f4 v[148:151], v[2:9], v[50:57], v[148:151], v1, v246 op_sel_hi:[0,0,0]
	v_mfma_scale_f32_16x16x128_f8f6f4 v[120:123], v[10:17], v[58:65], v[120:123], v1, v246 op_sel_hi:[0,0,0]
	v_mfma_scale_f32_16x16x128_f8f6f4 v[80:83], v[2:9], v[58:65], v[80:83], v1, v246 op_sel_hi:[0,0,0]
	s_setprio 0
	s_barrier
	s_add_i32 s4, s35, s8
	v_lshl_add_u64 v[250:251], v[240:241], 0, s[48:49]
	s_mov_b32 m0, s4
	ds_read_b128 v[58:61], v223 offset:49152
	ds_read_b128 v[62:65], v223 offset:50176
	ds_read_b128 v[50:53], v223 offset:51200
	ds_read_b128 v[54:57], v223 offset:52224
	ds_read_b128 v[42:45], v223 offset:53248
	ds_read_b128 v[46:49], v223 offset:54272
	ds_read_b128 v[34:37], v223 offset:55296
	ds_read_b128 v[38:41], v223 offset:56320
	global_load_lds_dwordx4 v[250:251], off
	v_lshl_add_u64 v[250:251], v[238:239], 0, s[48:49]
	s_add_i32 m0, s4, 0x2000
	s_add_i32 s4, s36, s8
	global_load_lds_dwordx4 v[250:251], off
	v_lshl_add_u64 v[240:241], v[240:241], 0, s[50:51]
	s_mov_b32 m0, s4
	v_lshl_add_u64 v[238:239], v[238:239], 0, s[50:51]
	global_load_lds_dwordx4 v[240:241], off
	s_add_i32 m0, s4, 0x2000
	s_andn2_b64 vcc, exec, s[90:91]
	global_load_lds_dwordx4 v[238:239], off
	v_lshl_add_u64 v[238:239], v[242:243], 0, s[48:49]
	s_mov_b32 m0, s20
	s_nop 0
	global_load_lds_dwordx4 v[238:239], off
	v_lshl_add_u64 v[238:239], v[244:245], 0, s[48:49]
	s_mov_b32 m0, s21
	s_nop 0
	global_load_lds_dwordx4 v[238:239], off
	s_waitcnt vmcnt(8)
	s_waitcnt lgkmcnt(0)
	s_barrier
	s_cbranch_vccnz .Lg2p_nf0
	s_setprio 1
	s_waitcnt lgkmcnt(0)
	v_mfma_scale_f32_16x16x128_f8f6f4 v[128:131], v[26:33], v[58:65], v[128:131], v1, v246 op_sel_hi:[0,0,0]
	v_med3_f32 v172, v172, s29, v227
	v_med3_f32 v173, v173, s29, v227
	v_med3_f32 v174, v174, s29, v227
	v_med3_f32 v175, v175, s29, v227
	v_cvt_pk_fp8_f32 v172, v172, v173
	v_cvt_pk_fp8_f32 v172, v174, v175 op_sel:[0,0,1]
	v_mfma_scale_f32_16x16x128_f8f6f4 v[124:127], v[18:25], v[58:65], v[124:127], v1, v246 op_sel_hi:[0,0,0]
	v_med3_f32 v176, v176, s29, v227
	v_med3_f32 v177, v177, s29, v227
	v_med3_f32 v178, v178, s29, v227
	v_med3_f32 v179, v179, s29, v227
	v_cvt_pk_fp8_f32 v173, v176, v177
	v_cvt_pk_fp8_f32 v173, v178, v179 op_sel:[0,0,1]
	v_mfma_scale_f32_16x16x128_f8f6f4 v[108:111], v[26:33], v[50:57], v[108:111], v1, v246 op_sel_hi:[0,0,0]
	v_med3_f32 v188, v188, s29, v227
	v_med3_f32 v189, v189, s29, v227
	v_med3_f32 v190, v190, s29, v227
	v_med3_f32 v191, v191, s29, v227
	v_cvt_pk_fp8_f32 v174, v188, v189
	v_cvt_pk_fp8_f32 v174, v190, v191 op_sel:[0,0,1]
	v_mfma_scale_f32_16x16x128_f8f6f4 v[104:107], v[18:25], v[50:57], v[104:107], v1, v246 op_sel_hi:[0,0,0]
	v_med3_f32 v192, v192, s29, v227
	v_med3_f32 v193, v193, s29, v227
	v_med3_f32 v194, v194, s29, v227
	v_med3_f32 v195, v195, s29, v227
	v_cvt_pk_fp8_f32 v175, v192, v193
	v_cvt_pk_fp8_f32 v175, v194, v195 op_sel:[0,0,1]
	v_mfma_scale_f32_16x16x128_f8f6f4 v[92:95], v[26:33], v[42:49], v[92:95], v1, v246 op_sel_hi:[0,0,0]
	v_med3_f32 v168, v168, s29, v227
	v_med3_f32 v169, v169, s29, v227
	v_med3_f32 v170, v170, s29, v227
	v_med3_f32 v171, v171, s29, v227
; #define PG8_STAGE(bufoff, gbase, voff) do { _Pragma("unroll") for (int _i = 0; _i < 2; ++_i) \
;         __builtin_amdgcn_global_load_lds((const unsigned*)((const char*)(gbase) + (voff)[_i]), (LAS unsigned*)(lds + (bufoff) + ldsw + _i * 8192), 16, 0, 0); } while (0)
; #define PG8_LDA(dst, b, h) do { _Pragma("unroll") for (int m = 0; m < 4; ++m) _Pragma("unroll") for (int k = 0; k < 2; ++k) dst[m][k] = *(const LAS bf16x8*)(lds + PG8_SA(b, h) + aoff + m * 2048 + k * 1024); } while (0)
; #define PG8_WAIT_V(n) asm volatile("s_waitcnt vmcnt(" #n ")" ::: "memory")
; #define PG8_WAIT_L(n) asm volatile("s_waitcnt lgkmcnt(" #n ")" ::: "memory")
; #define PG8_BAR __builtin_amdgcn_s_barrier()
; #define PG8_SCHED __builtin_amdgcn_sched_barrier(0)
;     ...
;             PG8_LDA(At, 1, 1); PG8_STAGE(PG8_SB(1, 0), b3, voffB); PG8_STAGE(PG8_SB(1, 1), b3 + bstep, voffB); PG8_STAGE(PG8_SA(1, 0), a3, v2[0]);
;             PG8_WAIT_V(8); PG8_WAIT_L(0); PG8_BAR; if (full) { PG8_MMA(1, 0, At, B0); PG8_MMA(1, 1, At, B1); } PG8_BAR; PG8_SCHED;
;     __device__ __forceinline__ u32x4 pack(const f32x4 (&acc)[2][2][4][2], int ai, int m) const {
;         u32x4 w;
; #pragma unroll
;         for (int bj = 0; bj < 2; ++bj) {
;             f32x4 v0 = acc[ai][bj][m][0], v1 = acc[ai][bj][m][1];
; #pragma unroll
;             for (int j = 0; j < 4; ++j) { v0[j] = fminf(fmaxf(v0[j], -448.f), 448.f); v1[j] = fminf(fmaxf(v1[j], -448.f), 448.f); }
;             int w0 = __builtin_amdgcn_cvt_pk_fp8_f32(v0[0], v0[1], 0, false); w0 = __builtin_amdgcn_cvt_pk_fp8_f32(v0[2], v0[3], w0, true);
;             int w1 = __builtin_amdgcn_cvt_pk_fp8_f32(v1[0], v1[1], 0, false); w1 = __builtin_amdgcn_cvt_pk_fp8_f32(v1[2], v1[3], w1, true);
;             if (bj == 0) { w.x = (unsigned)w0; w.y = (unsigned)w1; } else { w.z = (unsigned)w0; w.w = (unsigned)w1; } }
	v_cvt_pk_fp8_f32 v168, v168, v169
	v_cvt_pk_fp8_f32 v168, v170, v171 op_sel:[0,0,1]
	v_mfma_scale_f32_16x16x128_f8f6f4 v[84:87], v[18:25], v[42:49], v[84:87], v1, v246 op_sel_hi:[0,0,0]
	v_med3_f32 v164, v164, s29, v227
	v_med3_f32 v165, v165, s29, v227
	v_med3_f32 v166, v166, s29, v227
	v_med3_f32 v167, v167, s29, v227
	v_cvt_pk_fp8_f32 v169, v164, v165
	v_cvt_pk_fp8_f32 v169, v166, v167 op_sel:[0,0,1]
	v_mfma_scale_f32_16x16x128_f8f6f4 v[76:79], v[26:33], v[34:41], v[76:79], v1, v246 op_sel_hi:[0,0,0]
	v_med3_f32 v184, v184, s29, v227
	v_med3_f32 v185, v185, s29, v227
	v_med3_f32 v186, v186, s29, v227
	v_med3_f32 v187, v187, s29, v227
	v_cvt_pk_fp8_f32 v170, v184, v185
	v_cvt_pk_fp8_f32 v170, v186, v187 op_sel:[0,0,1]
	v_mfma_scale_f32_16x16x128_f8f6f4 v[72:75], v[18:25], v[34:41], v[72:75], v1, v246 op_sel_hi:[0,0,0]
	v_med3_f32 v180, v180, s29, v227
	v_med3_f32 v181, v181, s29, v227
	v_med3_f32 v182, v182, s29, v227
	v_med3_f32 v183, v183, s29, v227
	v_cvt_pk_fp8_f32 v171, v180, v181
	v_cvt_pk_fp8_f32 v171, v182, v183 op_sel:[0,0,1]
	s_setprio 0
	s_setprio 1
	v_mfma_scale_f32_16x16x128_f8f6f4 v[160:163], v[10:17], v[58:65], v[160:163], v1, v246 op_sel_hi:[0,0,0]
	v_med3_f32 v144, v144, s29, v227
	v_med3_f32 v145, v145, s29, v227
	v_med3_f32 v146, v146, s29, v227
	v_med3_f32 v147, v147, s29, v227
	v_cvt_pk_fp8_f32 v144, v144, v145
	v_cvt_pk_fp8_f32 v144, v146, v147 op_sel:[0,0,1]
	v_mfma_scale_f32_16x16x128_f8f6f4 v[156:159], v[2:9], v[58:65], v[156:159], v1, v246 op_sel_hi:[0,0,0]
	v_med3_f32 v136, v136, s29, v227
	v_med3_f32 v137, v137, s29, v227
	v_med3_f32 v138, v138, s29, v227
	v_med3_f32 v139, v139, s29, v227
	v_cvt_pk_fp8_f32 v145, v136, v137
	v_cvt_pk_fp8_f32 v145, v138, v139 op_sel:[0,0,1]
	v_mfma_scale_f32_16x16x128_f8f6f4 v[140:143], v[10:17], v[50:57], v[140:143], v1, v246 op_sel_hi:[0,0,0]
	v_med3_f32 v152, v152, s29, v227
	v_med3_f32 v153, v153, s29, v227
	v_med3_f32 v154, v154, s29, v227
	v_med3_f32 v155, v155, s29, v227
	v_cvt_pk_fp8_f32 v146, v152, v153
	v_cvt_pk_fp8_f32 v146, v154, v155 op_sel:[0,0,1]
	v_mfma_scale_f32_16x16x128_f8f6f4 v[132:135], v[2:9], v[50:57], v[132:135], v1, v246 op_sel_hi:[0,0,0]
	v_med3_f32 v148, v148, s29, v227
	v_med3_f32 v149, v149, s29, v227
	v_med3_f32 v150, v150, s29, v227
	v_med3_f32 v151, v151, s29, v227
	v_cvt_pk_fp8_f32 v147, v148, v149
	v_cvt_pk_fp8_f32 v147, v150, v151 op_sel:[0,0,1]
	v_mfma_scale_f32_16x16x128_f8f6f4 v[100:103], v[10:17], v[42:49], v[100:103], v1, v246 op_sel_hi:[0,0,0]
	v_med3_f32 v116, v116, s29, v227
	v_med3_f32 v117, v117, s29, v227
	v_med3_f32 v118, v118, s29, v227
	v_med3_f32 v119, v119, s29, v227
	v_cvt_pk_fp8_f32 v116, v116, v117
	v_cvt_pk_fp8_f32 v116, v118, v119 op_sel:[0,0,1]
	v_mfma_scale_f32_16x16x128_f8f6f4 v[96:99], v[2:9], v[42:49], v[96:99], v1, v246 op_sel_hi:[0,0,0]
	v_med3_f32 v112, v112, s29, v227
	v_med3_f32 v113, v113, s29, v227
	v_med3_f32 v114, v114, s29, v227
	v_med3_f32 v115, v115, s29, v227
	v_cvt_pk_fp8_f32 v117, v112, v113
	v_cvt_pk_fp8_f32 v117, v114, v115 op_sel:[0,0,1]
	v_mfma_scale_f32_16x16x128_f8f6f4 v[88:91], v[10:17], v[34:41], v[88:91], v1, v246 op_sel_hi:[0,0,0]
	v_med3_f32 v120, v120, s29, v227
	v_med3_f32 v121, v121, s29, v227
	v_med3_f32 v122, v122, s29, v227
	v_med3_f32 v123, v123, s29, v227
	v_cvt_pk_fp8_f32 v118, v120, v121
	v_cvt_pk_fp8_f32 v118, v122, v123 op_sel:[0,0,1]
	v_mfma_scale_f32_16x16x128_f8f6f4 v[68:71], v[2:9], v[34:41], v[68:71], v1, v246 op_sel_hi:[0,0,0]
	v_med3_f32 v80, v80, s29, v227
	v_med3_f32 v81, v81, s29, v227
	v_med3_f32 v82, v82, s29, v227
	v_med3_f32 v83, v83, s29, v227
	v_cvt_pk_fp8_f32 v119, v80, v81
	v_cvt_pk_fp8_f32 v119, v82, v83 op_sel:[0,0,1]
	s_setprio 0
	s_branch .LBB0_843
;     __device__ __forceinline__ u32x4 pack(const f32x4 (&acc)[2][2][4][2], int ai, int m) const {
;         u32x4 w;
; #pragma unroll
;         for (int bj = 0; bj < 2; ++bj) {
;             f32x4 v0 = acc[ai][bj][m][0], v1 = acc[ai][bj][m][1];
; #pragma unroll
;             for (int j = 0; j < 4; ++j) { v0[j] = fminf(fmaxf(v0[j], -448.f), 448.f); v1[j] = fminf(fmaxf(v1[j], -448.f), 448.f); }
;             int w0 = __builtin_amdgcn_cvt_pk_fp8_f32(v0[0], v0[1], 0, false); w0 = __builtin_amdgcn_cvt_pk_fp8_f32(v0[2], v0[3], w0, true);
;             int w1 = __builtin_amdgcn_cvt_pk_fp8_f32(v1[0], v1[1], 0, false); w1 = __builtin_amdgcn_cvt_pk_fp8_f32(v1[2], v1[3], w1, true);
;             if (bj == 0) { w.x = (unsigned)w0; w.y = (unsigned)w1; } else { w.z = (unsigned)w0; w.w = (unsigned)w1; } }
;         return w;
;     }
.Lg2p_nf0:
	v_med3_f32 v172, v172, s29, v227
	v_med3_f32 v173, v173, s29, v227
	v_med3_f32 v174, v174, s29, v227
	v_med3_f32 v175, v175, s29, v227
	v_cvt_pk_fp8_f32 v172, v172, v173
	v_cvt_pk_fp8_f32 v172, v174, v175 op_sel:[0,0,1]
	v_med3_f32 v176, v176, s29, v227
	v_med3_f32 v177, v177, s29, v227
	v_med3_f32 v178, v178, s29, v227
	v_med3_f32 v179, v179, s29, v227
	v_cvt_pk_fp8_f32 v173, v176, v177
	v_cvt_pk_fp8_f32 v173, v178, v179 op_sel:[0,0,1]
	v_med3_f32 v188, v188, s29, v227
	v_med3_f32 v189, v189, s29, v227
	v_med3_f32 v190, v190, s29, v227
	v_med3_f32 v191, v191, s29, v227
	v_cvt_pk_fp8_f32 v174, v188, v189
	v_cvt_pk_fp8_f32 v174, v190, v191 op_sel:[0,0,1]
	v_med3_f32 v192, v192, s29, v227
	v_med3_f32 v193, v193, s29, v227
	v_med3_f32 v194, v194, s29, v227
	v_med3_f32 v195, v195, s29, v227
	v_cvt_pk_fp8_f32 v175, v192, v193
	v_cvt_pk_fp8_f32 v175, v194, v195 op_sel:[0,0,1]
	v_med3_f32 v168, v168, s29, v227
	v_med3_f32 v169, v169, s29, v227
	v_med3_f32 v170, v170, s29, v227
	v_med3_f32 v171, v171, s29, v227
	v_cvt_pk_fp8_f32 v168, v168, v169
	v_cvt_pk_fp8_f32 v168, v170, v171 op_sel:[0,0,1]
	v_med3_f32 v164, v164, s29, v227
	v_med3_f32 v165, v165, s29, v227
	v_med3_f32 v166, v166, s29, v227
	v_med3_f32 v167, v167, s29, v227
	v_cvt_pk_fp8_f32 v169, v164, v165
	v_cvt_pk_fp8_f32 v169, v166, v167 op_sel:[0,0,1]
	v_med3_f32 v184, v184, s29, v227
	v_med3_f32 v185, v185, s29, v227
	v_med3_f32 v186, v186, s29, v227
	v_med3_f32 v187, v187, s29, v227
	v_cvt_pk_fp8_f32 v170, v184, v185
	v_cvt_pk_fp8_f32 v170, v186, v187 op_sel:[0,0,1]
	v_med3_f32 v180, v180, s29, v227
	v_med3_f32 v181, v181, s29, v227
	v_med3_f32 v182, v182, s29, v227
	v_med3_f32 v183, v183, s29, v227
	v_cvt_pk_fp8_f32 v171, v180, v181
	v_cvt_pk_fp8_f32 v171, v182, v183 op_sel:[0,0,1]
	v_med3_f32 v144, v144, s29, v227
	v_med3_f32 v145, v145, s29, v227
	v_med3_f32 v146, v146, s29, v227
	v_med3_f32 v147, v147, s29, v227
	v_cvt_pk_fp8_f32 v144, v144, v145
	v_cvt_pk_fp8_f32 v144, v146, v147 op_sel:[0,0,1]
	v_med3_f32 v136, v136, s29, v227
	v_med3_f32 v137, v137, s29, v227
	v_med3_f32 v138, v138, s29, v227
	v_med3_f32 v139, v139, s29, v227
	v_cvt_pk_fp8_f32 v145, v136, v137
	v_cvt_pk_fp8_f32 v145, v138, v139 op_sel:[0,0,1]
	v_med3_f32 v152, v152, s29, v227
	v_med3_f32 v153, v153, s29, v227
	v_med3_f32 v154, v154, s29, v227
	v_med3_f32 v155, v155, s29, v227
	v_cvt_pk_fp8_f32 v146, v152, v153
	v_cvt_pk_fp8_f32 v146, v154, v155 op_sel:[0,0,1]
	v_med3_f32 v148, v148, s29, v227
	v_med3_f32 v149, v149, s29, v227
	v_med3_f32 v150, v150, s29, v227
	v_med3_f32 v151, v151, s29, v227
	v_cvt_pk_fp8_f32 v147, v148, v149
	v_cvt_pk_fp8_f32 v147, v150, v151 op_sel:[0,0,1]
	v_med3_f32 v116, v116, s29, v227
	v_med3_f32 v117, v117, s29, v227
	v_med3_f32 v118, v118, s29, v227
	v_med3_f32 v119, v119, s29, v227
	v_cvt_pk_fp8_f32 v116, v116, v117
	v_cvt_pk_fp8_f32 v116, v118, v119 op_sel:[0,0,1]
	v_med3_f32 v112, v112, s29, v227
	v_med3_f32 v113, v113, s29, v227
	v_med3_f32 v114, v114, s29, v227
	v_med3_f32 v115, v115, s29, v227
	v_cvt_pk_fp8_f32 v117, v112, v113
	v_cvt_pk_fp8_f32 v117, v114, v115 op_sel:[0,0,1]
	v_med3_f32 v120, v120, s29, v227
	v_med3_f32 v121, v121, s29, v227
	v_med3_f32 v122, v122, s29, v227
	v_med3_f32 v123, v123, s29, v227
	v_cvt_pk_fp8_f32 v118, v120, v121
	v_cvt_pk_fp8_f32 v118, v122, v123 op_sel:[0,0,1]
	v_med3_f32 v80, v80, s29, v227
	v_med3_f32 v81, v81, s29, v227
	v_med3_f32 v82, v82, s29, v227
	v_med3_f32 v83, v83, s29, v227
	v_cvt_pk_fp8_f32 v119, v80, v81
	v_cvt_pk_fp8_f32 v119, v82, v83 op_sel:[0,0,1]

; #define LAS __attribute__((address_space(3)))
;     __device__ __forceinline__ void operator()(const f32x4 (&acc)[2][2][4][2], const Unit& u, int wr, int wc, int fr, int fq) const {
;     ...
;         { const u32x4 wa = pack(acc, 0, 0), wb = pack(acc, 0, 1); *(LAS u32x4*)(lds + B0 + wofs) = wa; *(LAS u32x4*)(lds + B0 + wofs + 16 * 256) = wb; }
; #pragma unroll
;         for (int sl = 0; sl < 4; ++sl) { const int ai = sl >> 1, mh = sl & 1;
;             asm volatile("s_waitcnt lgkmcnt(0)" ::: "memory"); __builtin_amdgcn_s_barrier();
;             const int rb = (sl & 1) ? B1 : B0, wb_ = (sl & 1) ? B0 : B1;
;             const u32x4 v0 = *(const LAS u32x4*)(lds + rb + rofs), v1 = *(const LAS u32x4*)(lds + rb + rofs4);
;             if (sl < 3) { const int a2 = (sl + 1) >> 1, m2 = ((sl + 1) & 1) * 2;
;                 const u32x4 wa = pack(acc, a2, m2), wb = pack(acc, a2, m2 + 1); *(LAS u32x4*)(lds + wb_ + wofs) = wa; *(LAS u32x4*)(lds + wb_ + wofs + 16 * 256) = wb; }
;             const int rl = ai * 128 + mh * 32 + t0;
;             if (!nost) { if (rl < u.nv) __builtin_nontemporal_store(v0, (u32x4*)(yp + (size_t)rl * D)); if (rl + 4 < u.nv) __builtin_nontemporal_store(v1, (u32x4*)(yp + (size_t)(rl + 4) * D)); } }
.LBB0_845:
	s_nop 15
	s_nop 15
	ds_write_b128 v207, v[172:175] offset:49152
	ds_write_b128 v207, v[168:171] offset:53248
	v_mov_b32_e32 v14, 0
	v_mov_b32_e32 v16, 0
	s_ashr_i32 s89, s88, 31
	s_lshl_b64 s[4:5], s[88:89], 10
	s_add_u32 s4, s18, s4
	s_addc_u32 s5, s19, s5
	s_lshl_b32 s34, s34, 8
	s_waitcnt lgkmcnt(0)
	s_barrier
	ds_read_b128 v[6:9], v231 offset:49152
	ds_read_b128 v[2:5], v235 offset:49152
	s_ashr_i32 s35, s34, 31
	s_add_u32 s4, s4, s34
	s_addc_u32 s5, s5, s35
	v_lshl_add_u64 v[10:11], s[4:5], 0, v[204:205]
	v_add_u32_e32 v12, 0x20410, v207
	v_cmp_gt_i32_e32 vcc, s7, v206
	ds_write_b128 v12, v[144:147]
	ds_write_b128 v211, v[116:119]
	s_and_saveexec_b64 s[4:5], vcc
	s_cbranch_execz .LBB0_847
	v_lshl_add_u64 v[14:15], v[10:11], 0, v[208:209]
	s_waitcnt lgkmcnt(0)
	global_store_dwordx4 v[14:15], v[6:9], off nt

; #define PG8_STAGE(bufoff, gbase, voff) do { _Pragma("unroll") for (int _i = 0; _i < 2; ++_i) \
;         __builtin_amdgcn_global_load_lds((const unsigned*)((const char*)(gbase) + (voff)[_i]), (LAS unsigned*)(lds + (bufoff) + ldsw + _i * 8192), 16, 0, 0); } while (0)
; #define PG8_LDA(dst, b, h) do { _Pragma("unroll") for (int m = 0; m < 4; ++m) _Pragma("unroll") for (int k = 0; k < 2; ++k) dst[m][k] = *(const LAS bf16x8*)(lds + PG8_SA(b, h) + aoff + m * 2048 + k * 1024); } while (0)
;     ...
;             if constexpr (SP2) {
;             PG8_LDB(B0, 0, 0); PG8_LDB(B1, 0, 1); PG8_SCHED; PG8_LDA(At, 0, 0); PG8_STAGE(PG8_SA(1, 1), a1 + ah, VA1);
;             PG8_WAIT_V(8); PG8_WAIT_L(0); PG8_BAR; PG8_MMA(0, 0, At, B0); PG8_MMA(0, 1, At, B1); PG8_BAR; PG8_SCHED;
;             PG8_LDA(At, 0, 1); PG8_STAGE(PG8_SB(0, 0), b2, voffB); PG8_STAGE(PG8_SB(0, 1), b2 + bstep, voffB); PG8_STAGE(PG8_SA(0, 0), a2, v2[0]);
;             PG8_WAIT_V(8); PG8_WAIT_L(0); PG8_BAR; if (full) { PG8_MMA(1, 0, At, B0); PG8_MMA(1, 1, At, B1); } PG8_BAR; PG8_SCHED;
;             PG8_LDB(B0, 1, 0); PG8_LDB(B1, 1, 1); PG8_SCHED; PG8_LDA(At, 1, 0); PG8_STAGE(PG8_SA(0, 1), a2 + ah, v2[1]);
;             PG8_WAIT_V(8); PG8_WAIT_L(0); PG8_BAR; PG8_MMA(0, 0, At, B0); PG8_MMA(0, 1, At, B1); PG8_BAR; PG8_SCHED;
;             PG8_LDA(At, 1, 1); PG8_STAGE(PG8_SB(1, 0), b3, voffB); PG8_STAGE(PG8_SB(1, 1), b3 + bstep, voffB); PG8_STAGE(PG8_SA(1, 0), a3, v2[0]);
;             PG8_WAIT_V(8); PG8_WAIT_L(0); PG8_BAR; if (full) { PG8_MMA(1, 0, At, B0); PG8_MMA(1, 1, At, B1); } PG8_BAR; PG8_SCHED;
;     __device__ __forceinline__ u32x4 pack(const f32x4 (&acc)[2][2][4][2], int ai, int m) const {
;         u32x4 w;
; #pragma unroll
;         for (int bj = 0; bj < 2; ++bj) {
;             f32x4 v0 = acc[ai][bj][m][0], v1 = acc[ai][bj][m][1];
; #pragma unroll
;             for (int j = 0; j < 4; ++j) { v0[j] = fminf(fmaxf(v0[j], -448.f), 448.f); v1[j] = fminf(fmaxf(v1[j], -448.f), 448.f); }
;             int w0 = __builtin_amdgcn_cvt_pk_fp8_f32(v0[0], v0[1], 0, false); w0 = __builtin_amdgcn_cvt_pk_fp8_f32(v0[2], v0[3], w0, true);
;             int w1 = __builtin_amdgcn_cvt_pk_fp8_f32(v1[0], v1[1], 0, false); w1 = __builtin_amdgcn_cvt_pk_fp8_f32(v1[2], v1[3], w1, true);
;             if (bj == 0) { w.x = (unsigned)w0; w.y = (unsigned)w1; } else { w.z = (unsigned)w0; w.w = (unsigned)w1; } }
.LBB0_1068:
	s_add_u32 s4, s4, 0x8000
	s_addc_u32 s5, s5, 0
	s_barrier
	s_add_i32 s18, 0, 0x18000
	s_add_i32 s19, 0, 0x1c000
	v_add_u32_e32 v2, s18, v247
	v_add_u32_e32 v6, s19, v247
	ds_read_b128 v[26:29], v2
	ds_read_b128 v[30:33], v2 offset:1024
	ds_read_b128 v[18:21], v2 offset:2048
	ds_read_b128 v[22:25], v2 offset:3072
	ds_read_b128 v[10:13], v6
	ds_read_b128 v[14:17], v6 offset:1024
	ds_read_b128 v[2:5], v6 offset:2048
	ds_read_b128 v[6:9], v6 offset:3072
	s_mov_b32 m0, s14
	v_lshl_add_u64 v[250:251], s[4:5], 0, v[200:201]
	s_waitcnt lgkmcnt(0)
	ds_read_b128 v[34:37], v223 offset:32768
	ds_read_b128 v[38:41], v223 offset:33792
	ds_read_b128 v[42:45], v223 offset:34816
	ds_read_b128 v[46:49], v223 offset:35840
	ds_read_b128 v[50:53], v223 offset:36864
	ds_read_b128 v[54:57], v223 offset:37888
	ds_read_b128 v[58:61], v223 offset:38912
	ds_read_b128 v[62:65], v223 offset:39936
	global_load_lds_dwordx4 v[250:251], off
	v_lshl_add_u64 v[250:251], s[4:5], 0, v[202:203]
	s_mov_b32 m0, s15
	s_nop 0
	global_load_lds_dwordx4 v[250:251], off
	s_waitcnt vmcnt(8)
	s_waitcnt lgkmcnt(0)
	s_barrier
	s_setprio 1
	s_waitcnt lgkmcnt(0)
	v_mfma_scale_f32_16x16x128_f8f6f4 v[172:175], v[26:33], v[34:41], v[172:175], v1, v246 op_sel_hi:[0,0,0]
	v_mfma_scale_f32_16x16x128_f8f6f4 v[176:179], v[18:25], v[34:41], v[176:179], v1, v246 op_sel_hi:[0,0,0]
	v_mfma_scale_f32_16x16x128_f8f6f4 v[168:171], v[26:33], v[42:49], v[168:171], v1, v246 op_sel_hi:[0,0,0]
	v_mfma_scale_f32_16x16x128_f8f6f4 v[164:167], v[18:25], v[42:49], v[164:167], v1, v246 op_sel_hi:[0,0,0]
	v_mfma_scale_f32_16x16x128_f8f6f4 v[144:147], v[26:33], v[50:57], v[144:147], v1, v246 op_sel_hi:[0,0,0]
	v_mfma_scale_f32_16x16x128_f8f6f4 v[136:139], v[18:25], v[50:57], v[136:139], v1, v246 op_sel_hi:[0,0,0]
	v_mfma_scale_f32_16x16x128_f8f6f4 v[116:119], v[26:33], v[58:65], v[116:119], v1, v246 op_sel_hi:[0,0,0]
	v_mfma_scale_f32_16x16x128_f8f6f4 v[112:115], v[18:25], v[58:65], v[112:115], v1, v246 op_sel_hi:[0,0,0]
	s_setprio 0
	s_setprio 1
	v_mfma_scale_f32_16x16x128_f8f6f4 v[188:191], v[10:17], v[34:41], v[188:191], v1, v246 op_sel_hi:[0,0,0]
	v_mfma_scale_f32_16x16x128_f8f6f4 v[192:195], v[2:9], v[34:41], v[192:195], v1, v246 op_sel_hi:[0,0,0]
	v_mfma_scale_f32_16x16x128_f8f6f4 v[184:187], v[10:17], v[42:49], v[184:187], v1, v246 op_sel_hi:[0,0,0]
	v_mfma_scale_f32_16x16x128_f8f6f4 v[180:183], v[2:9], v[42:49], v[180:183], v1, v246 op_sel_hi:[0,0,0]
	v_mfma_scale_f32_16x16x128_f8f6f4 v[152:155], v[10:17], v[50:57], v[152:155], v1, v246 op_sel_hi:[0,0,0]
	v_mfma_scale_f32_16x16x128_f8f6f4 v[148:151], v[2:9], v[50:57], v[148:151], v1, v246 op_sel_hi:[0,0,0]
	v_mfma_scale_f32_16x16x128_f8f6f4 v[120:123], v[10:17], v[58:65], v[120:123], v1, v246 op_sel_hi:[0,0,0]
	v_mfma_scale_f32_16x16x128_f8f6f4 v[80:83], v[2:9], v[58:65], v[80:83], v1, v246 op_sel_hi:[0,0,0]
	s_setprio 0
	s_barrier
	s_add_i32 s4, s18, s7
	v_lshl_add_u64 v[250:251], v[240:241], 0, s[48:49]
	s_mov_b32 m0, s4
	ds_read_b128 v[58:61], v223 offset:49152
	ds_read_b128 v[62:65], v223 offset:50176
	ds_read_b128 v[50:53], v223 offset:51200
	ds_read_b128 v[54:57], v223 offset:52224
	ds_read_b128 v[42:45], v223 offset:53248
	ds_read_b128 v[46:49], v223 offset:54272
	ds_read_b128 v[34:37], v223 offset:55296
	ds_read_b128 v[38:41], v223 offset:56320
	global_load_lds_dwordx4 v[250:251], off
	v_lshl_add_u64 v[250:251], v[238:239], 0, s[48:49]
	s_add_i32 m0, s4, 0x2000
	s_add_i32 s4, s19, s7
	global_load_lds_dwordx4 v[250:251], off
	v_lshl_add_u64 v[240:241], v[240:241], 0, s[50:51]
	s_mov_b32 m0, s4
	v_lshl_add_u64 v[238:239], v[238:239], 0, s[50:51]
	global_load_lds_dwordx4 v[240:241], off
	s_add_i32 m0, s4, 0x2000
	s_andn2_b64 vcc, exec, s[88:89]
	global_load_lds_dwordx4 v[238:239], off
	v_lshl_add_u64 v[238:239], v[242:243], 0, s[48:49]
	s_mov_b32 m0, s21
	s_nop 0
	global_load_lds_dwordx4 v[238:239], off
	v_lshl_add_u64 v[238:239], v[244:245], 0, s[48:49]
	s_mov_b32 m0, s22
	s_nop 0
	global_load_lds_dwordx4 v[238:239], off
	s_waitcnt vmcnt(8)
	s_waitcnt lgkmcnt(0)
	s_barrier
	s_cbranch_vccnz .Lg2p_nf1
	s_setprio 1
	s_waitcnt lgkmcnt(0)
	v_mfma_scale_f32_16x16x128_f8f6f4 v[128:131], v[26:33], v[58:65], v[128:131], v1, v246 op_sel_hi:[0,0,0]
	v_med3_f32 v172, v172, s30, v227
	v_med3_f32 v173, v173, s30, v227
	v_med3_f32 v174, v174, s30, v227
	v_med3_f32 v175, v175, s30, v227
	v_cvt_pk_fp8_f32 v172, v172, v173
	v_cvt_pk_fp8_f32 v172, v174, v175 op_sel:[0,0,1]
	v_mfma_scale_f32_16x16x128_f8f6f4 v[124:127], v[18:25], v[58:65], v[124:127], v1, v246 op_sel_hi:[0,0,0]
	v_med3_f32 v176, v176, s30, v227
	v_med3_f32 v177, v177, s30, v227
	v_med3_f32 v178, v178, s30, v227
	v_med3_f32 v179, v179, s30, v227
	v_cvt_pk_fp8_f32 v173, v176, v177
	v_cvt_pk_fp8_f32 v173, v178, v179 op_sel:[0,0,1]
	v_mfma_scale_f32_16x16x128_f8f6f4 v[108:111], v[26:33], v[50:57], v[108:111], v1, v246 op_sel_hi:[0,0,0]
	v_med3_f32 v188, v188, s30, v227
	v_med3_f32 v189, v189, s30, v227
	v_med3_f32 v190, v190, s30, v227
	v_med3_f32 v191, v191, s30, v227
	v_cvt_pk_fp8_f32 v174, v188, v189
	v_cvt_pk_fp8_f32 v174, v190, v191 op_sel:[0,0,1]
	v_mfma_scale_f32_16x16x128_f8f6f4 v[104:107], v[18:25], v[50:57], v[104:107], v1, v246 op_sel_hi:[0,0,0]
	v_med3_f32 v192, v192, s30, v227
	v_med3_f32 v193, v193, s30, v227
	v_med3_f32 v194, v194, s30, v227
	v_med3_f32 v195, v195, s30, v227
	v_cvt_pk_fp8_f32 v175, v192, v193
	v_cvt_pk_fp8_f32 v175, v194, v195 op_sel:[0,0,1]
	v_mfma_scale_f32_16x16x128_f8f6f4 v[92:95], v[26:33], v[42:49], v[92:95], v1, v246 op_sel_hi:[0,0,0]
	v_med3_f32 v168, v168, s30, v227
	v_med3_f32 v169, v169, s30, v227
	v_med3_f32 v170, v170, s30, v227
	v_med3_f32 v171, v171, s30, v227
; #define PG8_STAGE(bufoff, gbase, voff) do { _Pragma("unroll") for (int _i = 0; _i < 2; ++_i) \
;         __builtin_amdgcn_global_load_lds((const unsigned*)((const char*)(gbase) + (voff)[_i]), (LAS unsigned*)(lds + (bufoff) + ldsw + _i * 8192), 16, 0, 0); } while (0)
; #define PG8_LDA(dst, b, h) do { _Pragma("unroll") for (int m = 0; m < 4; ++m) _Pragma("unroll") for (int k = 0; k < 2; ++k) dst[m][k] = *(const LAS bf16x8*)(lds + PG8_SA(b, h) + aoff + m * 2048 + k * 1024); } while (0)
; #define PG8_WAIT_V(n) asm volatile("s_waitcnt vmcnt(" #n ")" ::: "memory")
; #define PG8_WAIT_L(n) asm volatile("s_waitcnt lgkmcnt(" #n ")" ::: "memory")
; #define PG8_BAR __builtin_amdgcn_s_barrier()
; #define PG8_SCHED __builtin_amdgcn_sched_barrier(0)
;     ...
;             PG8_LDA(At, 1, 1); PG8_STAGE(PG8_SB(1, 0), b3, voffB); PG8_STAGE(PG8_SB(1, 1), b3 + bstep, voffB); PG8_STAGE(PG8_SA(1, 0), a3, v2[0]);
;             PG8_WAIT_V(8); PG8_WAIT_L(0); PG8_BAR; if (full) { PG8_MMA(1, 0, At, B0); PG8_MMA(1, 1, At, B1); } PG8_BAR; PG8_SCHED;
;     __device__ __forceinline__ u32x4 pack(const f32x4 (&acc)[2][2][4][2], int ai, int m) const {
;         u32x4 w;
; #pragma unroll
;         for (int bj = 0; bj < 2; ++bj) {
;             f32x4 v0 = acc[ai][bj][m][0], v1 = acc[ai][bj][m][1];
; #pragma unroll
;             for (int j = 0; j < 4; ++j) { v0[j] = fminf(fmaxf(v0[j], -448.f), 448.f); v1[j] = fminf(fmaxf(v1[j], -448.f), 448.f); }
;             int w0 = __builtin_amdgcn_cvt_pk_fp8_f32(v0[0], v0[1], 0, false); w0 = __builtin_amdgcn_cvt_pk_fp8_f32(v0[2], v0[3], w0, true);
;             int w1 = __builtin_amdgcn_cvt_pk_fp8_f32(v1[0], v1[1], 0, false); w1 = __builtin_amdgcn_cvt_pk_fp8_f32(v1[2], v1[3], w1, true);
;             if (bj == 0) { w.x = (unsigned)w0; w.y = (unsigned)w1; } else { w.z = (unsigned)w0; w.w = (unsigned)w1; } }
	v_cvt_pk_fp8_f32 v168, v168, v169
	v_cvt_pk_fp8_f32 v168, v170, v171 op_sel:[0,0,1]
	v_mfma_scale_f32_16x16x128_f8f6f4 v[84:87], v[18:25], v[42:49], v[84:87], v1, v246 op_sel_hi:[0,0,0]
	v_med3_f32 v164, v164, s30, v227
	v_med3_f32 v165, v165, s30, v227
	v_med3_f32 v166, v166, s30, v227
	v_med3_f32 v167, v167, s30, v227
	v_cvt_pk_fp8_f32 v169, v164, v165
	v_cvt_pk_fp8_f32 v169, v166, v167 op_sel:[0,0,1]
	v_mfma_scale_f32_16x16x128_f8f6f4 v[76:79], v[26:33], v[34:41], v[76:79], v1, v246 op_sel_hi:[0,0,0]
	v_med3_f32 v184, v184, s30, v227
	v_med3_f32 v185, v185, s30, v227
	v_med3_f32 v186, v186, s30, v227
	v_med3_f32 v187, v187, s30, v227
	v_cvt_pk_fp8_f32 v170, v184, v185
	v_cvt_pk_fp8_f32 v170, v186, v187 op_sel:[0,0,1]
	v_mfma_scale_f32_16x16x128_f8f6f4 v[72:75], v[18:25], v[34:41], v[72:75], v1, v246 op_sel_hi:[0,0,0]
	v_med3_f32 v180, v180, s30, v227
	v_med3_f32 v181, v181, s30, v227
	v_med3_f32 v182, v182, s30, v227
	v_med3_f32 v183, v183, s30, v227
	v_cvt_pk_fp8_f32 v171, v180, v181
	v_cvt_pk_fp8_f32 v171, v182, v183 op_sel:[0,0,1]
	s_setprio 0
	s_setprio 1
	v_mfma_scale_f32_16x16x128_f8f6f4 v[160:163], v[10:17], v[58:65], v[160:163], v1, v246 op_sel_hi:[0,0,0]
	v_med3_f32 v144, v144, s30, v227
	v_med3_f32 v145, v145, s30, v227
	v_med3_f32 v146, v146, s30, v227
	v_med3_f32 v147, v147, s30, v227
	v_cvt_pk_fp8_f32 v144, v144, v145
	v_cvt_pk_fp8_f32 v144, v146, v147 op_sel:[0,0,1]
	v_mfma_scale_f32_16x16x128_f8f6f4 v[156:159], v[2:9], v[58:65], v[156:159], v1, v246 op_sel_hi:[0,0,0]
	v_med3_f32 v136, v136, s30, v227
	v_med3_f32 v137, v137, s30, v227
	v_med3_f32 v138, v138, s30, v227
	v_med3_f32 v139, v139, s30, v227
	v_cvt_pk_fp8_f32 v145, v136, v137
	v_cvt_pk_fp8_f32 v145, v138, v139 op_sel:[0,0,1]
	v_mfma_scale_f32_16x16x128_f8f6f4 v[140:143], v[10:17], v[50:57], v[140:143], v1, v246 op_sel_hi:[0,0,0]
	v_med3_f32 v152, v152, s30, v227
	v_med3_f32 v153, v153, s30, v227
	v_med3_f32 v154, v154, s30, v227
	v_med3_f32 v155, v155, s30, v227
	v_cvt_pk_fp8_f32 v146, v152, v153
	v_cvt_pk_fp8_f32 v146, v154, v155 op_sel:[0,0,1]
	v_mfma_scale_f32_16x16x128_f8f6f4 v[132:135], v[2:9], v[50:57], v[132:135], v1, v246 op_sel_hi:[0,0,0]
	v_med3_f32 v148, v148, s30, v227
	v_med3_f32 v149, v149, s30, v227
	v_med3_f32 v150, v150, s30, v227
	v_med3_f32 v151, v151, s30, v227
	v_cvt_pk_fp8_f32 v147, v148, v149
	v_cvt_pk_fp8_f32 v147, v150, v151 op_sel:[0,0,1]
	v_mfma_scale_f32_16x16x128_f8f6f4 v[100:103], v[10:17], v[42:49], v[100:103], v1, v246 op_sel_hi:[0,0,0]
	v_med3_f32 v116, v116, s30, v227
	v_med3_f32 v117, v117, s30, v227
	v_med3_f32 v118, v118, s30, v227
	v_med3_f32 v119, v119, s30, v227
	v_cvt_pk_fp8_f32 v116, v116, v117
	v_cvt_pk_fp8_f32 v116, v118, v119 op_sel:[0,0,1]
	v_mfma_scale_f32_16x16x128_f8f6f4 v[96:99], v[2:9], v[42:49], v[96:99], v1, v246 op_sel_hi:[0,0,0]
	v_med3_f32 v112, v112, s30, v227
	v_med3_f32 v113, v113, s30, v227
	v_med3_f32 v114, v114, s30, v227
	v_med3_f32 v115, v115, s30, v227
	v_cvt_pk_fp8_f32 v117, v112, v113
	v_cvt_pk_fp8_f32 v117, v114, v115 op_sel:[0,0,1]
	v_mfma_scale_f32_16x16x128_f8f6f4 v[88:91], v[10:17], v[34:41], v[88:91], v1, v246 op_sel_hi:[0,0,0]
	v_med3_f32 v120, v120, s30, v227
	v_med3_f32 v121, v121, s30, v227
	v_med3_f32 v122, v122, s30, v227
	v_med3_f32 v123, v123, s30, v227
	v_cvt_pk_fp8_f32 v118, v120, v121
	v_cvt_pk_fp8_f32 v118, v122, v123 op_sel:[0,0,1]
	v_mfma_scale_f32_16x16x128_f8f6f4 v[68:71], v[2:9], v[34:41], v[68:71], v1, v246 op_sel_hi:[0,0,0]
	v_med3_f32 v80, v80, s30, v227
	v_med3_f32 v81, v81, s30, v227
	v_med3_f32 v82, v82, s30, v227
	v_med3_f32 v83, v83, s30, v227
	v_cvt_pk_fp8_f32 v119, v80, v81
	v_cvt_pk_fp8_f32 v119, v82, v83 op_sel:[0,0,1]
	s_setprio 0
	s_branch .LBB0_1070
;     __device__ __forceinline__ u32x4 pack(const f32x4 (&acc)[2][2][4][2], int ai, int m) const {
;         u32x4 w;
; #pragma unroll
;         for (int bj = 0; bj < 2; ++bj) {
;             f32x4 v0 = acc[ai][bj][m][0], v1 = acc[ai][bj][m][1];
; #pragma unroll
;             for (int j = 0; j < 4; ++j) { v0[j] = fminf(fmaxf(v0[j], -448.f), 448.f); v1[j] = fminf(fmaxf(v1[j], -448.f), 448.f); }
;             int w0 = __builtin_amdgcn_cvt_pk_fp8_f32(v0[0], v0[1], 0, false); w0 = __builtin_amdgcn_cvt_pk_fp8_f32(v0[2], v0[3], w0, true);
;             int w1 = __builtin_amdgcn_cvt_pk_fp8_f32(v1[0], v1[1], 0, false); w1 = __builtin_amdgcn_cvt_pk_fp8_f32(v1[2], v1[3], w1, true);
;             if (bj == 0) { w.x = (unsigned)w0; w.y = (unsigned)w1; } else { w.z = (unsigned)w0; w.w = (unsigned)w1; } }
;         return w;
;     }
.Lg2p_nf1:
	v_med3_f32 v172, v172, s30, v227
	v_med3_f32 v173, v173, s30, v227
	v_med3_f32 v174, v174, s30, v227
	v_med3_f32 v175, v175, s30, v227
	v_cvt_pk_fp8_f32 v172, v172, v173
	v_cvt_pk_fp8_f32 v172, v174, v175 op_sel:[0,0,1]
	v_med3_f32 v176, v176, s30, v227
	v_med3_f32 v177, v177, s30, v227
	v_med3_f32 v178, v178, s30, v227
	v_med3_f32 v179, v179, s30, v227
	v_cvt_pk_fp8_f32 v173, v176, v177
	v_cvt_pk_fp8_f32 v173, v178, v179 op_sel:[0,0,1]
	v_med3_f32 v188, v188, s30, v227
	v_med3_f32 v189, v189, s30, v227
	v_med3_f32 v190, v190, s30, v227
	v_med3_f32 v191, v191, s30, v227
	v_cvt_pk_fp8_f32 v174, v188, v189
	v_cvt_pk_fp8_f32 v174, v190, v191 op_sel:[0,0,1]
	v_med3_f32 v192, v192, s30, v227
	v_med3_f32 v193, v193, s30, v227
	v_med3_f32 v194, v194, s30, v227
	v_med3_f32 v195, v195, s30, v227
	v_cvt_pk_fp8_f32 v175, v192, v193
	v_cvt_pk_fp8_f32 v175, v194, v195 op_sel:[0,0,1]
	v_med3_f32 v168, v168, s30, v227
	v_med3_f32 v169, v169, s30, v227
	v_med3_f32 v170, v170, s30, v227
	v_med3_f32 v171, v171, s30, v227
	v_cvt_pk_fp8_f32 v168, v168, v169
	v_cvt_pk_fp8_f32 v168, v170, v171 op_sel:[0,0,1]
	v_med3_f32 v164, v164, s30, v227
	v_med3_f32 v165, v165, s30, v227
	v_med3_f32 v166, v166, s30, v227
	v_med3_f32 v167, v167, s30, v227
	v_cvt_pk_fp8_f32 v169, v164, v165
	v_cvt_pk_fp8_f32 v169, v166, v167 op_sel:[0,0,1]
	v_med3_f32 v184, v184, s30, v227
	v_med3_f32 v185, v185, s30, v227
	v_med3_f32 v186, v186, s30, v227
	v_med3_f32 v187, v187, s30, v227
	v_cvt_pk_fp8_f32 v170, v184, v185
	v_cvt_pk_fp8_f32 v170, v186, v187 op_sel:[0,0,1]
	v_med3_f32 v180, v180, s30, v227
	v_med3_f32 v181, v181, s30, v227
	v_med3_f32 v182, v182, s30, v227
	v_med3_f32 v183, v183, s30, v227
	v_cvt_pk_fp8_f32 v171, v180, v181
	v_cvt_pk_fp8_f32 v171, v182, v183 op_sel:[0,0,1]
	v_med3_f32 v144, v144, s30, v227
	v_med3_f32 v145, v145, s30, v227
	v_med3_f32 v146, v146, s30, v227
	v_med3_f32 v147, v147, s30, v227
	v_cvt_pk_fp8_f32 v144, v144, v145
	v_cvt_pk_fp8_f32 v144, v146, v147 op_sel:[0,0,1]
	v_med3_f32 v136, v136, s30, v227
	v_med3_f32 v137, v137, s30, v227
	v_med3_f32 v138, v138, s30, v227
	v_med3_f32 v139, v139, s30, v227
	v_cvt_pk_fp8_f32 v145, v136, v137
	v_cvt_pk_fp8_f32 v145, v138, v139 op_sel:[0,0,1]
	v_med3_f32 v152, v152, s30, v227
	v_med3_f32 v153, v153, s30, v227
	v_med3_f32 v154, v154, s30, v227
	v_med3_f32 v155, v155, s30, v227
	v_cvt_pk_fp8_f32 v146, v152, v153
	v_cvt_pk_fp8_f32 v146, v154, v155 op_sel:[0,0,1]
	v_med3_f32 v148, v148, s30, v227
	v_med3_f32 v149, v149, s30, v227
	v_med3_f32 v150, v150, s30, v227
	v_med3_f32 v151, v151, s30, v227
	v_cvt_pk_fp8_f32 v147, v148, v149
	v_cvt_pk_fp8_f32 v147, v150, v151 op_sel:[0,0,1]
	v_med3_f32 v116, v116, s30, v227
	v_med3_f32 v117, v117, s30, v227
	v_med3_f32 v118, v118, s30, v227
	v_med3_f32 v119, v119, s30, v227
	v_cvt_pk_fp8_f32 v116, v116, v117
	v_cvt_pk_fp8_f32 v116, v118, v119 op_sel:[0,0,1]
	v_med3_f32 v112, v112, s30, v227
	v_med3_f32 v113, v113, s30, v227
	v_med3_f32 v114, v114, s30, v227
	v_med3_f32 v115, v115, s30, v227
	v_cvt_pk_fp8_f32 v117, v112, v113
	v_cvt_pk_fp8_f32 v117, v114, v115 op_sel:[0,0,1]
	v_med3_f32 v120, v120, s30, v227
	v_med3_f32 v121, v121, s30, v227
	v_med3_f32 v122, v122, s30, v227
	v_med3_f32 v123, v123, s30, v227
	v_cvt_pk_fp8_f32 v118, v120, v121
	v_cvt_pk_fp8_f32 v118, v122, v123 op_sel:[0,0,1]
	v_med3_f32 v80, v80, s30, v227
	v_med3_f32 v81, v81, s30, v227
	v_med3_f32 v82, v82, s30, v227
	v_med3_f32 v83, v83, s30, v227
	v_cvt_pk_fp8_f32 v119, v80, v81
	v_cvt_pk_fp8_f32 v119, v82, v83 op_sel:[0,0,1]

; #define LAS __attribute__((address_space(3)))
;     __device__ __forceinline__ void operator()(const f32x4 (&acc)[2][2][4][2], const Unit& u, int wr, int wc, int fr, int fq) const {
;     ...
;         { const u32x4 wa = pack(acc, 0, 0), wb = pack(acc, 0, 1); *(LAS u32x4*)(lds + B0 + wofs) = wa; *(LAS u32x4*)(lds + B0 + wofs + 16 * 256) = wb; }
; #pragma unroll
;         for (int sl = 0; sl < 4; ++sl) { const int ai = sl >> 1, mh = sl & 1;
;             asm volatile("s_waitcnt lgkmcnt(0)" ::: "memory"); __builtin_amdgcn_s_barrier();
;             const int rb = (sl & 1) ? B1 : B0, wb_ = (sl & 1) ? B0 : B1;
;             const u32x4 v0 = *(const LAS u32x4*)(lds + rb + rofs), v1 = *(const LAS u32x4*)(lds + rb + rofs4);
;             if (sl < 3) { const int a2 = (sl + 1) >> 1, m2 = ((sl + 1) & 1) * 2;
;                 const u32x4 wa = pack(acc, a2, m2), wb = pack(acc, a2, m2 + 1); *(LAS u32x4*)(lds + wb_ + wofs) = wa; *(LAS u32x4*)(lds + wb_ + wofs + 16 * 256) = wb; }
;             const int rl = ai * 128 + mh * 32 + t0;
;             if (!nost) { if (rl < u.nv) __builtin_nontemporal_store(v0, (u32x4*)(yp + (size_t)rl * D)); if (rl + 4 < u.nv) __builtin_nontemporal_store(v1, (u32x4*)(yp + (size_t)(rl + 4) * D)); } }
.LBB0_1072:
	s_nop 15
	s_nop 15
	ds_write_b128 v207, v[172:175] offset:49152
	ds_write_b128 v207, v[168:171] offset:53248
	v_mov_b32_e32 v14, 0
	v_mov_b32_e32 v16, 0
	s_ashr_i32 s87, s86, 31
	s_lshl_b64 s[4:5], s[86:87], 10
	s_add_u32 s4, s17, s4
	s_addc_u32 s5, s20, s5
	s_lshl_b32 s18, s34, 8
	s_waitcnt lgkmcnt(0)
	s_barrier
	ds_read_b128 v[6:9], v231 offset:49152
	ds_read_b128 v[2:5], v235 offset:49152
	s_ashr_i32 s19, s18, 31
	s_add_u32 s4, s4, s18
	s_addc_u32 s5, s5, s19
	v_lshl_add_u64 v[10:11], s[4:5], 0, v[204:205]
	v_add_u32_e32 v12, 0x20410, v207
	v_cmp_gt_i32_e32 vcc, s6, v206
	ds_write_b128 v12, v[144:147]
	ds_write_b128 v211, v[116:119]
	s_and_saveexec_b64 s[4:5], vcc
	s_cbranch_execz .LBB0_1074
	v_lshl_add_u64 v[14:15], v[10:11], 0, v[208:209]
	s_waitcnt lgkmcnt(0)
	global_store_dwordx4 v[14:15], v[6:9], off nt
